# speedup vs baseline: 1.0143x; 1.0105x over previous
_Z11gram_kernelPKfPKiS0_S0_S0_S0_S0_S0_S0_S0_S0_Pf:
	s_load_dwordx4 s[24:27], s[0:1], 0x0
	s_load_dwordx2 s[28:29], s[0:1], 0x40
	s_load_dwordx4 s[20:23], s[0:1], 0x30
	s_load_dwordx2 s[10:11], s[0:1], 0x58
	s_load_dwordx2 s[44:45], s[0:1], 0x20
	s_load_dwordx2 s[68:69], s[0:1], 0x10
	s_load_dwordx2 s[60:61], s[0:1], 0x18
	s_load_dwordx2 s[62:63], s[0:1], 0x28
	s_load_dwordx2 s[64:65], s[0:1], 0x48
	s_load_dwordx2 s[66:67], s[0:1], 0x50
	s_ashr_i32 s30, s2, 1
	v_mov_b32_e32 v11, 0
	s_ashr_i32 s31, s30, 31
	s_lshl_b32 s46, s30, 11
	s_lshl_b32 s3, s2, 10
	s_ashr_i32 s47, s46, 31
	s_and_b32 s33, s3, 0x400
	v_lshlrev_b32_e32 v46, 2, v0
	v_mov_b32_e32 v47, 0
	v_lshlrev_b32_e32 v212, 1, v0
	v_mov_b32_e32 v213, v47
	v_lshrrev_b32_e32 v219, 6, v0
	v_bfe_u32 v214, v0, 5, 1
	v_and_b32_e32 v220, 31, v0
	s_or_b32 s3, s46, s33
	v_lshlrev_b32_e32 v216, 4, v219
	v_lshlrev_b32_e32 v221, 3, v214
	v_or3_b32 v1, s3, v216, v221
	v_lshlrev_b32_e32 v232, 4, v220
	v_and_b32_e32 v218, 63, v0
	s_mov_b32 s39, 0x20000
	s_brev_b32 s38, 16
	v_lshl_or_b32 v180, v1, 9, v232
	v_add_u32_e32 v1, 0x10000, v180
	s_lshl_b64 s[4:5], s[46:47], 2
	s_lshl_b32 s3, s33, 2
	s_lshl_b64 s[6:7], s[30:31], 14
	s_waitcnt lgkmcnt(0)
	s_add_u32 s48, s20, s6
	s_addc_u32 s49, s21, s7
	s_mov_b64 s[36:37], s[24:25]
	s_and_b32 s37, s37, 0xffff
	s_add_u32 s26, s26, s4
	s_addc_u32 s27, s27, s5
	s_add_u32 s26, s26, s3
	s_addc_u32 s27, s27, 0
	v_lshl_add_u64 v[32:33], v[212:213], 2, s[26:27]
	global_load_dwordx2 v[32:33], v[32:33], off
	buffer_load_dwordx4 v[34:37], v180, s[36:39], 0 offen sc1 nt
	buffer_load_dwordx4 v[38:41], v180, s[36:39], 0 offen offset:512 sc1 nt
	buffer_load_dwordx4 v[42:45], v180, s[36:39], 0 offen offset:1024 sc1 nt
	buffer_load_dwordx4 v[96:99], v180, s[36:39], 0 offen offset:1536 sc1 nt
	buffer_load_dwordx4 v[100:103], v180, s[36:39], 0 offen offset:2048 sc1 nt
	buffer_load_dwordx4 v[104:107], v180, s[36:39], 0 offen offset:2560 sc1 nt
	buffer_load_dwordx4 v[108:111], v180, s[36:39], 0 offen offset:3072 sc1 nt
	buffer_load_dwordx4 v[112:115], v180, s[36:39], 0 offen offset:3584 sc1 nt
	global_load_dword v250, v47, s[22:23]
	global_load_dword v250, v47, s[28:29]
	global_load_dword v250, v47, s[68:69]
	global_load_dword v250, v47, s[44:45]
	global_load_dword v250, v47, s[48:49]
	global_load_dword v250, v47, s[60:61]
	global_load_dword v250, v47, s[62:63]
	global_load_dword v250, v47, s[64:65]
	global_load_dword v250, v47, s[66:67]
	buffer_load_dwordx4 v[116:119], v1, s[36:39], 0 offen sc1 nt
	buffer_load_dwordx4 v[120:123], v1, s[36:39], 0 offen offset:512 sc1 nt
	buffer_load_dwordx4 v[124:127], v1, s[36:39], 0 offen offset:1024 sc1 nt
	buffer_load_dwordx4 v[128:131], v1, s[36:39], 0 offen offset:1536 sc1 nt
	buffer_load_dwordx4 v[132:135], v1, s[36:39], 0 offen offset:2048 sc1 nt
	buffer_load_dwordx4 v[136:139], v1, s[36:39], 0 offen offset:2560 sc1 nt
	buffer_load_dwordx4 v[140:143], v1, s[36:39], 0 offen offset:3072 sc1 nt
	buffer_load_dwordx4 v[144:147], v1, s[36:39], 0 offen offset:3584 sc1 nt
	s_movk_i32 s3, 0x160
	v_cmp_gt_u32_e32 vcc, s3, v0
	s_mov_b32 s3, 0x10000
	v_lshrrev_b32_e32 v227, 5, v0
	v_and_b32_e32 v228, 0x7c, v46
	v_add_u32_e32 v2, 0x200, v0
	v_lshrrev_b32_e32 v229, 5, v2
	v_mul_u32_u24_e32 v246, 0x110, v227
	v_lshl_add_u32 v246, v220, 3, v246
	v_add_u32_e32 v246, 0x10000, v246
	v_lshlrev_b32_e32 v247, 2, v46
	s_waitcnt vmcnt(25)
	v_cmp_ne_u32_e64 s[6:7], 0, v32
	v_cmp_ne_u32_e64 s[4:5], 0, v33
	v_cmp_eq_u32_e64 s[8:9], 0, v218
	s_nop 0
	s_and_saveexec_b64 s[12:13], s[8:9]
	s_cbranch_execz .LBB0_6
	s_bcnt1_i32_b64 s6, s[6:7]
	s_bcnt1_i32_b64 s4, s[4:5]
	v_mov_b32_e32 v1, 0x21100
	s_add_i32 s4, s4, s6
	v_lshl_add_u32 v1, v219, 2, v1
	v_mov_b32_e32 v2, s4
	ds_write_b32 v1, v2

.LBB0_11:
	s_add_i32 s3, s3, 2
	s_cmp_gt_u32 s3, 5
	s_cselect_b64 vcc, -1, 0
	v_add_u32_e32 v184, 0xffff0000, v183
	s_and_b64 s[12:13], vcc, exec
	v_cndmask_b32_e32 v200, v184, v1, vcc
	s_cselect_b32 s15, 0x20000, 0x20000
	s_cselect_b32 s14, 0x10000, s16
	s_cselect_b32 s13, s41, s37
	s_cselect_b32 s12, s22, s36
	s_waitcnt vmcnt(8)
	v_cvt_pk_f16_f32 v187, v172, v176
	v_cvt_pk_f16_f32 v186, v160, v168
	v_cvt_pk_f16_f32 v185, v164, v156
	v_cvt_pk_f16_f32 v184, v148, v152
	v_cvt_pk_f16_f32 v191, v173, v177
	v_cvt_pk_f16_f32 v190, v161, v169
	v_cvt_pk_f16_f32 v189, v165, v157
	v_cvt_pk_f16_f32 v188, v149, v153
	v_cvt_pk_f16_f32 v195, v174, v178
	v_cvt_pk_f16_f32 v194, v162, v170
	v_cvt_pk_f16_f32 v193, v166, v158
	v_cvt_pk_f16_f32 v192, v150, v154
	v_cvt_pk_f16_f32 v199, v175, v179
	v_cvt_pk_f16_f32 v198, v163, v171
	v_cvt_pk_f16_f32 v197, v167, v159
	v_cvt_pk_f16_f32 v196, v151, v155
	buffer_load_dwordx4 v[148:151], v200, s[12:15], 0 offen sc1 nt
	buffer_load_dwordx4 v[152:155], v200, s[12:15], 0 offen offset:512 sc1 nt
	buffer_load_dwordx4 v[164:167], v200, s[12:15], 0 offen offset:1024 sc1 nt
	buffer_load_dwordx4 v[156:159], v200, s[12:15], 0 offen offset:1536 sc1 nt
	buffer_load_dwordx4 v[160:163], v200, s[12:15], 0 offen offset:2048 sc1 nt
	buffer_load_dwordx4 v[168:171], v200, s[12:15], 0 offen offset:2560 sc1 nt
	buffer_load_dwordx4 v[172:175], v200, s[12:15], 0 offen offset:3072 sc1 nt
	buffer_load_dwordx4 v[176:179], v200, s[12:15], 0 offen offset:3584 sc1 nt
	ds_write_b128 v180, v[184:187]
	ds_write_b128 v180, v[188:191] offset:1024
	ds_write_b128 v180, v[192:195] offset:2048
	ds_write_b128 v180, v[196:199] offset:3072
	s_cselect_b32 s14, s17, 0x8000000
	s_cselect_b32 s13, s29, s37
	s_cselect_b32 s12, s28, s36
	v_cndmask_b32_e32 v200, v183, v1, vcc
	s_cmp_lg_u32 s3, 0
	s_cbranch_scc1 .Lw47_not0
	global_load_dwordx4 v[48:51], v247, s[68:69]
	global_load_dwordx4 v[80:83], v247, s[44:45]
	v_add_u32_e32 v247, 0x2000, v247
	global_load_dwordx4 v[52:55], v247, s[68:69]
	global_load_dwordx4 v[84:87], v247, s[44:45]
	v_add_u32_e32 v247, 0x2000, v247
	global_load_dwordx4 v[56:59], v247, s[68:69]
	global_load_dwordx4 v[88:91], v247, s[44:45]
	v_add_u32_e32 v247, 0x2000, v247
	global_load_dwordx4 v[60:63], v247, s[68:69]
	global_load_dwordx4 v[92:95], v247, s[44:45]
	v_add_u32_e32 v247, 0x2000, v247
	global_load_dwordx4 v[64:67], v247, s[68:69]
	global_load_dwordx4 v[96:99], v247, s[44:45]
	v_add_u32_e32 v247, 0x2000, v247
	global_load_dwordx4 v[68:71], v247, s[68:69]
	global_load_dwordx4 v[100:103], v247, s[44:45]
	v_add_u32_e32 v247, 0x2000, v247
	global_load_dwordx4 v[72:75], v247, s[68:69]
	global_load_dwordx4 v[104:107], v247, s[44:45]
	v_add_u32_e32 v247, 0x2000, v247
	global_load_dwordx4 v[76:79], v247, s[68:69]
	global_load_dwordx4 v[108:111], v247, s[44:45]
	s_branch .Lw47_xdone

.Lw47_wdone:
	v_cvt_pk_f16_f32 v187, v140, v144
	v_cvt_pk_f16_f32 v186, v132, v136
	v_cvt_pk_f16_f32 v185, v124, v128
	v_cvt_pk_f16_f32 v184, v116, v120
	v_cvt_pk_f16_f32 v191, v141, v145
	v_cvt_pk_f16_f32 v190, v133, v137
	v_cvt_pk_f16_f32 v189, v125, v129
	v_cvt_pk_f16_f32 v188, v117, v121
	v_cvt_pk_f16_f32 v195, v142, v146
	v_cvt_pk_f16_f32 v194, v134, v138
	v_cvt_pk_f16_f32 v193, v126, v130
	v_cvt_pk_f16_f32 v192, v118, v122
	v_cvt_pk_f16_f32 v199, v143, v147
	v_cvt_pk_f16_f32 v198, v135, v139
	v_cvt_pk_f16_f32 v197, v127, v131
	v_cvt_pk_f16_f32 v196, v119, v123
	buffer_load_dwordx4 v[116:119], v200, s[12:15], 0 offen sc1 nt
	buffer_load_dwordx4 v[120:123], v200, s[12:15], 0 offen offset:512 sc1 nt
	buffer_load_dwordx4 v[124:127], v200, s[12:15], 0 offen offset:1024 sc1 nt
	buffer_load_dwordx4 v[128:131], v200, s[12:15], 0 offen offset:1536 sc1 nt
	buffer_load_dwordx4 v[132:135], v200, s[12:15], 0 offen offset:2048 sc1 nt
	buffer_load_dwordx4 v[136:139], v200, s[12:15], 0 offen offset:2560 sc1 nt
	buffer_load_dwordx4 v[140:143], v200, s[12:15], 0 offen offset:3072 sc1 nt
	buffer_load_dwordx4 v[144:147], v200, s[12:15], 0 offen offset:3584 sc1 nt
	ds_write_b128 v180, v[184:187] offset:32768
	ds_write_b128 v180, v[188:191] offset:33792
	ds_write_b128 v180, v[192:195] offset:34816
	ds_write_b128 v180, v[196:199] offset:35840
	s_waitcnt lgkmcnt(0)
	s_barrier
	ds_read_b128 v[184:187], v181 offset:32768
	ds_read_b128 v[188:191], v182 offset:32768
	ds_read_b128 v[192:195], v182 offset:33792
	ds_read_b128 v[196:199], v181 offset:36864
	s_waitcnt lgkmcnt(2)
	v_mfma_f32_32x32x16_f16 v[18:33], v[184:187], v[188:191], v[18:33]
	v_add_u32_e32 v183, 0x20000, v183
	s_cmp_lt_u32 s3, 6
	s_waitcnt lgkmcnt(1)
	v_mfma_f32_32x32x16_f16 v[2:17], v[184:187], v[192:195], v[2:17]
	ds_read_b128 v[184:187], v182 offset:36864
	ds_read_b128 v[188:191], v182 offset:37888
	s_waitcnt lgkmcnt(1)
	v_mfma_f32_32x32x16_f16 v[18:33], v[196:199], v[184:187], v[18:33]
	s_waitcnt lgkmcnt(0)
	v_mfma_f32_32x32x16_f16 v[2:17], v[196:199], v[188:191], v[2:17]
	ds_read_b128 v[184:187], v181 offset:40960
	ds_read_b128 v[188:191], v182 offset:40960
	ds_read_b128 v[192:195], v182 offset:41984
	ds_read_b128 v[196:199], v181 offset:45056
	s_waitcnt lgkmcnt(2)
	v_mfma_f32_32x32x16_f16 v[18:33], v[184:187], v[188:191], v[18:33]
	s_waitcnt lgkmcnt(1)
	v_mfma_f32_32x32x16_f16 v[2:17], v[184:187], v[192:195], v[2:17]
	ds_read_b128 v[184:187], v182 offset:45056
	ds_read_b128 v[188:191], v182 offset:46080
	s_waitcnt lgkmcnt(1)
	v_mfma_f32_32x32x16_f16 v[18:33], v[196:199], v[184:187], v[18:33]
	s_waitcnt lgkmcnt(0)
	v_mfma_f32_32x32x16_f16 v[2:17], v[196:199], v[188:191], v[2:17]
	ds_read_b128 v[184:187], v181 offset:49152
	ds_read_b128 v[188:191], v182 offset:49152
	ds_read_b128 v[192:195], v182 offset:50176
	ds_read_b128 v[196:199], v181 offset:53248
	s_waitcnt lgkmcnt(2)
	v_mfma_f32_32x32x16_f16 v[18:33], v[184:187], v[188:191], v[18:33]
	s_waitcnt lgkmcnt(1)
	v_mfma_f32_32x32x16_f16 v[2:17], v[184:187], v[192:195], v[2:17]
	ds_read_b128 v[184:187], v182 offset:53248
	ds_read_b128 v[188:191], v182 offset:54272
	s_waitcnt lgkmcnt(1)
	v_mfma_f32_32x32x16_f16 v[18:33], v[196:199], v[184:187], v[18:33]
	s_waitcnt lgkmcnt(0)
	v_mfma_f32_32x32x16_f16 v[2:17], v[196:199], v[188:191], v[2:17]
	ds_read_b128 v[184:187], v181 offset:57344
	ds_read_b128 v[188:191], v182 offset:57344
	ds_read_b128 v[192:195], v182 offset:58368
	ds_read_b128 v[196:199], v181 offset:61440
	s_waitcnt lgkmcnt(2)
	v_mfma_f32_32x32x16_f16 v[18:33], v[184:187], v[188:191], v[18:33]
	s_waitcnt lgkmcnt(1)
	v_mfma_f32_32x32x16_f16 v[2:17], v[184:187], v[192:195], v[2:17]
	ds_read_b128 v[184:187], v182 offset:61440
	ds_read_b128 v[188:191], v182 offset:62464
	s_waitcnt lgkmcnt(1)
	v_mfma_f32_32x32x16_f16 v[18:33], v[196:199], v[184:187], v[18:33]
	s_waitcnt lgkmcnt(0)
	v_mfma_f32_32x32x16_f16 v[2:17], v[196:199], v[188:191], v[2:17]
	s_cbranch_scc1 .LBB0_11
.LBB0_13:
	s_or_saveexec_b64 s[10:11], s[10:11]
	v_mov_b32_e32 v217, 0
	s_xor_b64 exec, exec, s[10:11]
	s_cbranch_execz .LBB0_19
	s_nop 6
	v_add_u32_e32 v2, 0x20000, v180
	buffer_load_dwordx4 v[148:151], v2, s[36:39], 0 offen sc1 nt
	buffer_load_dwordx4 v[152:155], v2, s[36:39], 0 offen offset:512 sc1 nt
	buffer_load_dwordx4 v[164:167], v2, s[36:39], 0 offen offset:1024 sc1 nt
	buffer_load_dwordx4 v[156:159], v2, s[36:39], 0 offen offset:1536 sc1 nt
	buffer_load_dwordx4 v[160:163], v2, s[36:39], 0 offen offset:2048 sc1 nt
	buffer_load_dwordx4 v[168:171], v2, s[36:39], 0 offen offset:2560 sc1 nt
	buffer_load_dwordx4 v[172:175], v2, s[36:39], 0 offen offset:3072 sc1 nt
	buffer_load_dwordx4 v[176:179], v2, s[36:39], 0 offen offset:3584 sc1 nt
	v_lshlrev_b32_e32 v233, 4, v218
	s_waitcnt vmcnt(16)
	v_cvt_pk_f16_f32 v5, v108, v112
	v_cvt_pk_f16_f32 v4, v100, v104
	v_cvt_pk_f16_f32 v3, v42, v96
	v_cvt_pk_f16_f32 v2, v34, v38
	v_lshl_or_b32 v234, v219, 12, v233
	ds_write_b128 v234, v[2:5]
	v_cvt_pk_f16_f32 v5, v109, v113
	v_cvt_pk_f16_f32 v4, v101, v105
	v_cvt_pk_f16_f32 v3, v43, v97
	v_cvt_pk_f16_f32 v2, v35, v39
	ds_write_b128 v234, v[2:5] offset:1024
	v_cvt_pk_f16_f32 v5, v110, v114
	v_cvt_pk_f16_f32 v4, v102, v106
	v_cvt_pk_f16_f32 v3, v44, v98
	v_cvt_pk_f16_f32 v2, v36, v40
	s_movk_i32 s12, 0xf400
	ds_write_b128 v234, v[2:5] offset:2048
	v_cvt_pk_f16_f32 v5, v111, v115
	v_cvt_pk_f16_f32 v4, v103, v107
	v_cvt_pk_f16_f32 v3, v45, v99
	v_cvt_pk_f16_f32 v2, v37, v41
	v_mad_i32_i24 v235, v219, s12, v234
	s_add_i32 s12, s46, s33
	ds_write_b128 v234, v[2:5] offset:3072
	global_load_dwordx4 v[48:51], v247, s[68:69]
	global_load_dwordx4 v[80:83], v247, s[44:45]
	v_add_u32_e32 v247, 0x2000, v247
	global_load_dwordx4 v[52:55], v247, s[68:69]
	global_load_dwordx4 v[84:87], v247, s[44:45]
	v_add_u32_e32 v247, 0x2000, v247
	global_load_dwordx4 v[56:59], v247, s[68:69]
	global_load_dwordx4 v[88:91], v247, s[44:45]
	v_add_u32_e32 v247, 0x2000, v247
	global_load_dwordx4 v[60:63], v247, s[68:69]
	global_load_dwordx4 v[92:95], v247, s[44:45]
	v_add_u32_e32 v247, 0x2000, v247
	global_load_dwordx4 v[64:67], v247, s[68:69]
	global_load_dwordx4 v[96:99], v247, s[44:45]
	v_add_u32_e32 v247, 0x2000, v247
	global_load_dwordx4 v[68:71], v247, s[68:69]
	global_load_dwordx4 v[100:103], v247, s[44:45]
	v_add_u32_e32 v247, 0x2000, v247
	global_load_dwordx4 v[72:75], v247, s[68:69]
	global_load_dwordx4 v[104:107], v247, s[44:45]
	v_add_u32_e32 v247, 0x2000, v247
	global_load_dwordx4 v[76:79], v247, s[68:69]
	global_load_dwordx4 v[108:111], v247, s[44:45]
	v_add3_u32 v2, s12, v216, v221
	v_lshl_or_b32 v2, v2, 9, v232
	v_mov_b32_e32 v217, 0
	s_mov_b32 s3, 0
	v_add_u32_e32 v236, 0x40000, v2
	s_mov_b32 s16, 0x10000
	v_mov_b32_e32 v2, v217
	v_mov_b32_e32 v3, v217
	v_mov_b32_e32 v4, v217
	v_mov_b32_e32 v5, v217
	v_mov_b32_e32 v6, v217
	v_mov_b32_e32 v7, v217
	v_mov_b32_e32 v8, v217
	v_mov_b32_e32 v9, v217
	v_mov_b32_e32 v10, v217
	v_mov_b32_e32 v11, v217
	v_mov_b32_e32 v12, v217
	v_mov_b32_e32 v13, v217
	v_mov_b32_e32 v14, v217
	v_mov_b32_e32 v15, v217
	v_mov_b32_e32 v16, v217
	v_mov_b32_e32 v17, v217
	v_mov_b32_e32 v18, v217
	v_mov_b32_e32 v19, v217
	v_mov_b32_e32 v20, v217
	v_mov_b32_e32 v21, v217
	v_mov_b32_e32 v22, v217
	v_mov_b32_e32 v23, v217
	v_mov_b32_e32 v24, v217
	v_mov_b32_e32 v25, v217
	v_mov_b32_e32 v26, v217
	v_mov_b32_e32 v27, v217
	v_mov_b32_e32 v28, v217
	v_mov_b32_e32 v29, v217
	v_mov_b32_e32 v30, v217
	v_mov_b32_e32 v31, v217
	v_mov_b32_e32 v32, v217
	v_mov_b32_e32 v33, v217
	s_branch .LBB0_16
.LBB0_15:
	s_cmp_gt_u32 s3, 3
	s_cselect_b64 vcc, -1, 0
	s_and_b64 s[14:15], vcc, exec
	s_waitcnt vmcnt(8)
	v_cndmask_b32_e32 v176, v236, v1, vcc
	s_cselect_b32 s55, 0x20000, 0x20000
	s_cselect_b32 s54, s16, 0x8000000
	s_cselect_b32 s53, s41, s37
	s_cselect_b32 s52, s22, s36
	buffer_load_dwordx4 v[148:151], v176, s[52:55], 0 offen sc1 nt
	buffer_load_dwordx4 v[152:155], v176, s[52:55], 0 offen offset:512 sc1 nt
	buffer_load_dwordx4 v[164:167], v176, s[52:55], 0 offen offset:1024 sc1 nt
	buffer_load_dwordx4 v[156:159], v176, s[52:55], 0 offen offset:1536 sc1 nt
	buffer_load_dwordx4 v[160:163], v176, s[52:55], 0 offen offset:2048 sc1 nt
	buffer_load_dwordx4 v[168:171], v176, s[52:55], 0 offen offset:2560 sc1 nt
	buffer_load_dwordx4 v[172:175], v176, s[52:55], 0 offen offset:3072 sc1 nt
	s_nop 0
	buffer_load_dwordx4 v[176:179], v176, s[52:55], 0 offen offset:3584 sc1 nt
	v_dot2c_f32_f16_e32 v217, 0x3c003c00, v180
	v_dot2c_f32_f16_e32 v217, 0x3c003c00, v181
	v_dot2c_f32_f16_e32 v217, 0x3c003c00, v182
	v_dot2c_f32_f16_e32 v217, 0x3c003c00, v183
	v_dot2c_f32_f16_e32 v217, 0x3c003c00, v184
	v_dot2c_f32_f16_e32 v217, 0x3c003c00, v185
	v_dot2c_f32_f16_e32 v217, 0x3c003c00, v186
	v_dot2c_f32_f16_e32 v217, 0x3c003c00, v187
	v_dot2c_f32_f16_e32 v217, 0x3c003c00, v188
	v_dot2c_f32_f16_e32 v217, 0x3c003c00, v189
	v_dot2c_f32_f16_e32 v217, 0x3c003c00, v190
	v_dot2c_f32_f16_e32 v217, 0x3c003c00, v191
	v_dot2c_f32_f16_e32 v217, 0x3c003c00, v192
	v_dot2c_f32_f16_e32 v217, 0x3c003c00, v193
	v_dot2c_f32_f16_e32 v217, 0x3c003c00, v194
	v_dot2c_f32_f16_e32 v217, 0x3c003c00, v195
	v_dot2c_f32_f16_e32 v217, 0x3c003c00, v196
	v_dot2c_f32_f16_e32 v217, 0x3c003c00, v197
	v_dot2c_f32_f16_e32 v217, 0x3c003c00, v198
	v_dot2c_f32_f16_e32 v217, 0x3c003c00, v199
	v_dot2c_f32_f16_e32 v217, 0x3c003c00, v200
	v_dot2c_f32_f16_e32 v217, 0x3c003c00, v201
	v_dot2c_f32_f16_e32 v217, 0x3c003c00, v202
	v_dot2c_f32_f16_e32 v217, 0x3c003c00, v203
	v_dot2c_f32_f16_e32 v217, 0x3c003c00, v204
	v_dot2c_f32_f16_e32 v217, 0x3c003c00, v205
	v_dot2c_f32_f16_e32 v217, 0x3c003c00, v206
	v_dot2c_f32_f16_e32 v217, 0x3c003c00, v207
	v_dot2c_f32_f16_e32 v217, 0x3c003c00, v208
	v_dot2c_f32_f16_e32 v217, 0x3c003c00, v209
	v_dot2c_f32_f16_e32 v217, 0x3c003c00, v210
	v_dot2c_f32_f16_e32 v217, 0x3c003c00, v211
	s_add_i32 s3, s3, 2
	ds_read_b128 v[180:183], v235 offset:32768
	ds_read_b128 v[184:187], v233 offset:32768
	ds_read_b128 v[188:191], v233 offset:33792
	ds_read_b128 v[192:195], v235 offset:36864
	v_add_u32_e32 v236, 0x20000, v236
	s_waitcnt lgkmcnt(3)
	v_dot2c_f32_f16_e32 v217, 0x3c003c00, v180
	s_waitcnt lgkmcnt(2)
	v_mfma_f32_32x32x16_f16 v[18:33], v[180:183], v[184:187], v[18:33]
	v_dot2c_f32_f16_e32 v217, 0x3c003c00, v181
	v_dot2c_f32_f16_e32 v217, 0x3c003c00, v182
	v_dot2c_f32_f16_e32 v217, 0x3c003c00, v183
	s_waitcnt lgkmcnt(0)
	v_dot2c_f32_f16_e32 v217, 0x3c003c00, v192
	v_dot2c_f32_f16_e32 v217, 0x3c003c00, v193
	v_dot2c_f32_f16_e32 v217, 0x3c003c00, v194
	v_dot2c_f32_f16_e32 v217, 0x3c003c00, v195
	v_mfma_f32_32x32x16_f16 v[2:17], v[180:183], v[188:191], v[2:17]
	ds_read_b128 v[184:187], v233 offset:36864
	ds_read_b128 v[188:191], v233 offset:37888
	s_and_b64 vcc, exec, s[12:13]
	s_waitcnt lgkmcnt(1)
	v_mfma_f32_32x32x16_f16 v[18:33], v[192:195], v[184:187], v[18:33]
	s_waitcnt lgkmcnt(0)
	v_mfma_f32_32x32x16_f16 v[2:17], v[192:195], v[188:191], v[2:17]
	ds_read_b128 v[184:187], v235 offset:40960
	ds_read_b128 v[188:191], v233 offset:40960
	ds_read_b128 v[196:199], v233 offset:41984
	ds_read_b128 v[200:203], v235 offset:45056
	s_waitcnt lgkmcnt(3)
	v_dot2c_f32_f16_e32 v217, 0x3c003c00, v184
	v_dot2c_f32_f16_e32 v217, 0x3c003c00, v185
	v_dot2c_f32_f16_e32 v217, 0x3c003c00, v186
	v_dot2c_f32_f16_e32 v217, 0x3c003c00, v187
	s_waitcnt lgkmcnt(0)
	v_dot2c_f32_f16_e32 v217, 0x3c003c00, v200
	v_mfma_f32_32x32x16_f16 v[18:33], v[184:187], v[188:191], v[18:33]
	v_dot2c_f32_f16_e32 v217, 0x3c003c00, v201
	v_dot2c_f32_f16_e32 v217, 0x3c003c00, v202
	v_dot2c_f32_f16_e32 v217, 0x3c003c00, v203
	v_mfma_f32_32x32x16_f16 v[2:17], v[184:187], v[196:199], v[2:17]
	ds_read_b128 v[188:191], v233 offset:45056
	ds_read_b128 v[196:199], v233 offset:46080
	s_waitcnt lgkmcnt(1)
	v_mfma_f32_32x32x16_f16 v[18:33], v[200:203], v[188:191], v[18:33]
	s_waitcnt lgkmcnt(0)
	v_mfma_f32_32x32x16_f16 v[2:17], v[200:203], v[196:199], v[2:17]
	ds_read_b128 v[188:191], v235 offset:49152
	ds_read_b128 v[196:199], v233 offset:49152
	ds_read_b128 v[204:207], v233 offset:50176
	ds_read_b128 v[208:211], v235 offset:53248
	ds_read_b128 v[180:183], v233 offset:54272
	ds_read_b128 v[192:195], v235 offset:57344
	s_waitcnt lgkmcnt(5)
	v_dot2c_f32_f16_e32 v217, 0x3c003c00, v188
	v_dot2c_f32_f16_e32 v217, 0x3c003c00, v189
	v_dot2c_f32_f16_e32 v217, 0x3c003c00, v190
	v_dot2c_f32_f16_e32 v217, 0x3c003c00, v191
	s_waitcnt lgkmcnt(4)
	v_mfma_f32_32x32x16_f16 v[18:33], v[188:191], v[196:199], v[18:33]
	ds_read_b128 v[196:199], v233 offset:53248
	s_waitcnt lgkmcnt(3)
	v_dot2c_f32_f16_e32 v217, 0x3c003c00, v208
	v_dot2c_f32_f16_e32 v217, 0x3c003c00, v209
	v_dot2c_f32_f16_e32 v217, 0x3c003c00, v210
	v_dot2c_f32_f16_e32 v217, 0x3c003c00, v211
	v_mfma_f32_32x32x16_f16 v[2:17], v[188:191], v[204:207], v[2:17]
	s_waitcnt lgkmcnt(0)
	v_mfma_f32_32x32x16_f16 v[18:33], v[208:211], v[196:199], v[18:33]
	v_mfma_f32_32x32x16_f16 v[2:17], v[208:211], v[180:183], v[2:17]
	ds_read_b128 v[180:183], v233 offset:57344
	ds_read_b128 v[184:187], v233 offset:58368
	ds_read_b128 v[196:199], v235 offset:61440
	v_dot2c_f32_f16_e32 v217, 0x3c003c00, v192
	v_dot2c_f32_f16_e32 v217, 0x3c003c00, v193
	v_dot2c_f32_f16_e32 v217, 0x3c003c00, v194
	v_dot2c_f32_f16_e32 v217, 0x3c003c00, v195
	s_waitcnt lgkmcnt(0)
	v_dot2c_f32_f16_e32 v217, 0x3c003c00, v196
	v_mfma_f32_32x32x16_f16 v[18:33], v[192:195], v[180:183], v[18:33]
	ds_read_b128 v[180:183], v233 offset:61440
	v_dot2c_f32_f16_e32 v217, 0x3c003c00, v197
	v_dot2c_f32_f16_e32 v217, 0x3c003c00, v198
	v_dot2c_f32_f16_e32 v217, 0x3c003c00, v199
	v_mfma_f32_32x32x16_f16 v[2:17], v[192:195], v[184:187], v[2:17]
	ds_read_b128 v[184:187], v233 offset:62464
	s_waitcnt lgkmcnt(1)
	v_mfma_f32_32x32x16_f16 v[18:33], v[196:199], v[180:183], v[18:33]
	s_waitcnt lgkmcnt(0)
	v_mfma_f32_32x32x16_f16 v[2:17], v[196:199], v[184:187], v[2:17]
	s_cbranch_vccnz .LBB0_19

.Lw03_wdone:
	v_cvt_pk_f16_f32 v183, v140, v144
	v_cvt_pk_f16_f32 v182, v132, v136
	v_cvt_pk_f16_f32 v181, v124, v128
	v_cvt_pk_f16_f32 v180, v116, v120
	v_cvt_pk_f16_f32 v187, v141, v145
	v_cvt_pk_f16_f32 v186, v133, v137
	v_cvt_pk_f16_f32 v185, v125, v129
	v_cvt_pk_f16_f32 v184, v117, v121
	v_cvt_pk_f16_f32 v191, v142, v146
	v_cvt_pk_f16_f32 v190, v134, v138
	v_cvt_pk_f16_f32 v189, v126, v130
	v_cvt_pk_f16_f32 v188, v118, v122
	v_cvt_pk_f16_f32 v195, v143, v147
	v_cvt_pk_f16_f32 v194, v135, v139
	v_cvt_pk_f16_f32 v193, v127, v131
	v_cvt_pk_f16_f32 v192, v119, v123
	buffer_load_dwordx4 v[116:119], v196, s[12:15], 0 offen sc1 nt
	buffer_load_dwordx4 v[120:123], v196, s[12:15], 0 offen offset:512 sc1 nt
	buffer_load_dwordx4 v[124:127], v196, s[12:15], 0 offen offset:1024 sc1 nt
	buffer_load_dwordx4 v[128:131], v196, s[12:15], 0 offen offset:1536 sc1 nt
	buffer_load_dwordx4 v[132:135], v196, s[12:15], 0 offen offset:2048 sc1 nt
	buffer_load_dwordx4 v[136:139], v196, s[12:15], 0 offen offset:2560 sc1 nt
	buffer_load_dwordx4 v[140:143], v196, s[12:15], 0 offen offset:3072 sc1 nt
	buffer_load_dwordx4 v[144:147], v196, s[12:15], 0 offen offset:3584 sc1 nt
	ds_write_b128 v234, v[180:183] offset:32768
	ds_write_b128 v234, v[184:187] offset:33792
	ds_write_b128 v234, v[188:191] offset:34816
	ds_write_b128 v234, v[192:195] offset:35840
	ds_read_b128 v[180:183], v235
	ds_read_b128 v[188:191], v233
	ds_read_b128 v[192:195], v233 offset:1024
	ds_read_b128 v[184:187], v235 offset:4096
	s_waitcnt lgkmcnt(2)
	v_mfma_f32_32x32x16_f16 v[18:33], v[180:183], v[188:191], v[18:33]
	s_waitcnt lgkmcnt(1)
	v_mfma_f32_32x32x16_f16 v[2:17], v[180:183], v[192:195], v[2:17]
	ds_read_b128 v[188:191], v233 offset:4096
	ds_read_b128 v[192:195], v233 offset:5120
	s_waitcnt lgkmcnt(1)
	v_mfma_f32_32x32x16_f16 v[18:33], v[184:187], v[188:191], v[18:33]
	s_waitcnt lgkmcnt(0)
	v_mfma_f32_32x32x16_f16 v[2:17], v[184:187], v[192:195], v[2:17]
	ds_read_b128 v[188:191], v235 offset:8192
	ds_read_b128 v[196:199], v233 offset:8192
	ds_read_b128 v[200:203], v233 offset:9216
	ds_read_b128 v[192:195], v235 offset:12288
	s_waitcnt lgkmcnt(2)
	v_mfma_f32_32x32x16_f16 v[18:33], v[188:191], v[196:199], v[18:33]
	s_waitcnt lgkmcnt(1)
	v_mfma_f32_32x32x16_f16 v[2:17], v[188:191], v[200:203], v[2:17]
	ds_read_b128 v[196:199], v233 offset:12288
	ds_read_b128 v[200:203], v233 offset:13312
	s_waitcnt lgkmcnt(1)
	v_mfma_f32_32x32x16_f16 v[18:33], v[192:195], v[196:199], v[18:33]
	s_waitcnt lgkmcnt(0)
	v_mfma_f32_32x32x16_f16 v[2:17], v[192:195], v[200:203], v[2:17]
	ds_read_b128 v[196:199], v235 offset:16384
	ds_read_b128 v[204:207], v233 offset:16384
	ds_read_b128 v[208:211], v233 offset:17408
	ds_read_b128 v[200:203], v235 offset:20480
	s_waitcnt lgkmcnt(2)
	v_mfma_f32_32x32x16_f16 v[18:33], v[196:199], v[204:207], v[18:33]
	s_waitcnt lgkmcnt(1)
	v_mfma_f32_32x32x16_f16 v[2:17], v[196:199], v[208:211], v[2:17]
	ds_read_b128 v[204:207], v233 offset:20480
	ds_read_b128 v[208:211], v233 offset:21504
	s_waitcnt lgkmcnt(1)
	v_mfma_f32_32x32x16_f16 v[18:33], v[200:203], v[204:207], v[18:33]
	s_waitcnt lgkmcnt(0)
	v_mfma_f32_32x32x16_f16 v[2:17], v[200:203], v[208:211], v[2:17]
	ds_read_b128 v[204:207], v235 offset:24576
	ds_read_b128 v[238:241], v233 offset:24576
	ds_read_b128 v[242:245], v233 offset:25600
	ds_read_b128 v[208:211], v235 offset:28672
	s_waitcnt lgkmcnt(2)
	v_mfma_f32_32x32x16_f16 v[18:33], v[204:207], v[238:241], v[18:33]
	s_waitcnt lgkmcnt(1)
	v_mfma_f32_32x32x16_f16 v[2:17], v[204:207], v[242:245], v[2:17]
	ds_read_b128 v[238:241], v233 offset:28672
	ds_read_b128 v[242:245], v233 offset:29696
	s_waitcnt lgkmcnt(1)
	v_mfma_f32_32x32x16_f16 v[18:33], v[208:211], v[238:241], v[18:33]
	s_waitcnt lgkmcnt(0)
	v_mfma_f32_32x32x16_f16 v[2:17], v[208:211], v[242:245], v[2:17]
	s_cmp_gt_u32 s3, 5
	s_cselect_b64 s[12:13], -1, 0
	s_and_b64 vcc, exec, s[12:13]
	s_barrier
	s_cbranch_vccnz .LBB0_15
	s_waitcnt vmcnt(8)
	v_cvt_pk_f16_f32 v241, v172, v176
	v_cvt_pk_f16_f32 v240, v160, v168
	v_cvt_pk_f16_f32 v239, v164, v156
	v_cvt_pk_f16_f32 v238, v148, v152
	ds_write_b128 v234, v[238:241]
	v_cvt_pk_f16_f32 v241, v173, v177
	v_cvt_pk_f16_f32 v240, v161, v169
	v_cvt_pk_f16_f32 v239, v165, v157
	v_cvt_pk_f16_f32 v238, v149, v153
	ds_write_b128 v234, v[238:241] offset:1024
	v_cvt_pk_f16_f32 v241, v174, v178
	v_cvt_pk_f16_f32 v240, v162, v170
	v_cvt_pk_f16_f32 v239, v166, v158
	v_cvt_pk_f16_f32 v238, v150, v154
	v_cvt_pk_f16_f32 v161, v175, v179
	v_cvt_pk_f16_f32 v160, v163, v171
	v_cvt_pk_f16_f32 v159, v167, v159
	v_cvt_pk_f16_f32 v158, v151, v155
	ds_write_b128 v234, v[238:241] offset:2048
	ds_write_b128 v234, v[158:161] offset:3072
	s_cmp_lg_u32 s3, 0
	s_cbranch_scc1 .LBB0_15
	v_cvt_pk_f16_f32 v48, v48, v49
	v_cvt_pk_f16_f32 v49, v50, v51
	ds_write_b64 v246, v[48:49]
	v_cvt_pk_f16_f32 v80, v80, v81
	v_cvt_pk_f16_f32 v81, v82, v83
	ds_write_b64 v246, v[80:81] offset:34816
	v_cvt_pk_f16_f32 v52, v52, v53
	v_cvt_pk_f16_f32 v53, v54, v55
	ds_write_b64 v246, v[52:53] offset:4352
	v_cvt_pk_f16_f32 v84, v84, v85
	v_cvt_pk_f16_f32 v85, v86, v87
	ds_write_b64 v246, v[84:85] offset:39168
	v_cvt_pk_f16_f32 v56, v56, v57
	v_cvt_pk_f16_f32 v57, v58, v59
	ds_write_b64 v246, v[56:57] offset:8704
	v_cvt_pk_f16_f32 v88, v88, v89
	v_cvt_pk_f16_f32 v89, v90, v91
	ds_write_b64 v246, v[88:89] offset:43520
	v_cvt_pk_f16_f32 v60, v60, v61
	v_cvt_pk_f16_f32 v61, v62, v63
	ds_write_b64 v246, v[60:61] offset:13056
	v_cvt_pk_f16_f32 v92, v92, v93
	v_cvt_pk_f16_f32 v93, v94, v95
	ds_write_b64 v246, v[92:93] offset:47872
	v_cvt_pk_f16_f32 v64, v64, v65
	v_cvt_pk_f16_f32 v65, v66, v67
	ds_write_b64 v246, v[64:65] offset:17408
	v_cvt_pk_f16_f32 v96, v96, v97
	v_cvt_pk_f16_f32 v97, v98, v99
	ds_write_b64 v246, v[96:97] offset:52224
	v_cvt_pk_f16_f32 v68, v68, v69
	v_cvt_pk_f16_f32 v69, v70, v71
	ds_write_b64 v246, v[68:69] offset:21760
	v_cvt_pk_f16_f32 v100, v100, v101
	v_cvt_pk_f16_f32 v101, v102, v103
	ds_write_b64 v246, v[100:101] offset:56576
	v_cvt_pk_f16_f32 v72, v72, v73
	v_cvt_pk_f16_f32 v73, v74, v75
	ds_write_b64 v246, v[72:73] offset:26112
	v_cvt_pk_f16_f32 v104, v104, v105
	v_cvt_pk_f16_f32 v105, v106, v107
	ds_write_b64 v246, v[104:105] offset:60928
	v_cvt_pk_f16_f32 v76, v76, v77
	v_cvt_pk_f16_f32 v77, v78, v79
	ds_write_b64 v246, v[76:77] offset:30464
	v_cvt_pk_f16_f32 v108, v108, v109
	v_cvt_pk_f16_f32 v109, v110, v111
	ds_write_b64 v246, v[108:109] offset:65280
	s_branch .LBB0_15

.LBB0_24:
	s_cmp_eq_u32 s3, 0
	s_cbranch_scc1 .LBB0_23
	v_add_u32_e32 v112, s3, v118
	buffer_load_dwordx4 v[34:37], v112, s[36:39], 0 offen sc1 nt
	buffer_load_dwordx4 v[38:41], v112, s[36:39], 0 offen offset:512 sc1 nt
	buffer_load_dwordx4 v[42:45], v112, s[36:39], 0 offen offset:1024 sc1 nt
	buffer_load_dwordx4 v[96:99], v112, s[36:39], 0 offen offset:1536 sc1 nt
	buffer_load_dwordx4 v[100:103], v112, s[36:39], 0 offen offset:2048 sc1 nt
	buffer_load_dwordx4 v[104:107], v112, s[36:39], 0 offen offset:2560 sc1 nt
	buffer_load_dwordx4 v[108:111], v112, s[36:39], 0 offen offset:3072 sc1 nt
	s_nop 0
	buffer_load_dwordx4 v[112:115], v112, s[36:39], 0 offen offset:3584 sc1 nt
	s_branch .LBB0_23

.LBB0_30:
	s_cmp_eq_u32 s23, 0
	s_cbranch_scc1 .LBB0_29
	v_add_u32_e32 v112, s23, v119
	buffer_load_dwordx4 v[34:37], v112, s[36:39], 0 offen sc1 nt
	buffer_load_dwordx4 v[38:41], v112, s[36:39], 0 offen offset:512 sc1 nt
	buffer_load_dwordx4 v[42:45], v112, s[36:39], 0 offen offset:1024 sc1 nt
	buffer_load_dwordx4 v[96:99], v112, s[36:39], 0 offen offset:1536 sc1 nt
	buffer_load_dwordx4 v[100:103], v112, s[36:39], 0 offen offset:2048 sc1 nt
	buffer_load_dwordx4 v[104:107], v112, s[36:39], 0 offen offset:2560 sc1 nt
	buffer_load_dwordx4 v[108:111], v112, s[36:39], 0 offen offset:3072 sc1 nt
	s_nop 0
	buffer_load_dwordx4 v[112:115], v112, s[36:39], 0 offen offset:3584 sc1 nt
	s_branch .LBB0_29
.LBB0_32:
	s_or_b64 exec, exec, s[20:21]
	s_mov_b32 s40, s22
	s_mov_b32 s30, s42
	s_mov_b32 s31, s43
	buffer_load_dwordx4 v[148:151], v1, s[40:43], 0 offen sc1 nt
	buffer_load_dwordx4 v[152:155], v1, s[40:43], 0 offen offset:512 sc1 nt
	buffer_load_dwordx4 v[116:119], v1, s[28:31], 0 offen sc1 nt
	buffer_load_dwordx4 v[120:123], v1, s[28:31], 0 offen offset:512 sc1 nt
	buffer_load_dwordx4 v[164:167], v1, s[40:43], 0 offen offset:1024 sc1 nt
	buffer_load_dwordx4 v[156:159], v1, s[40:43], 0 offen offset:1536 sc1 nt
	buffer_load_dwordx4 v[124:127], v1, s[28:31], 0 offen offset:1024 sc1 nt
	buffer_load_dwordx4 v[128:131], v1, s[28:31], 0 offen offset:1536 sc1 nt
	buffer_load_dwordx4 v[160:163], v1, s[40:43], 0 offen offset:2048 sc1 nt
	buffer_load_dwordx4 v[168:171], v1, s[40:43], 0 offen offset:2560 sc1 nt
	buffer_load_dwordx4 v[132:135], v1, s[28:31], 0 offen offset:2048 sc1 nt
	buffer_load_dwordx4 v[136:139], v1, s[28:31], 0 offen offset:2560 sc1 nt
	buffer_load_dwordx4 v[172:175], v1, s[40:43], 0 offen offset:3072 sc1 nt
	buffer_load_dwordx4 v[176:179], v1, s[40:43], 0 offen offset:3584 sc1 nt
	buffer_load_dwordx4 v[140:143], v1, s[28:31], 0 offen offset:3072 sc1 nt
	buffer_load_dwordx4 v[144:147], v1, s[28:31], 0 offen offset:3584 sc1 nt
